# v3 + all small fixes stacked: row-table loads batched, router pass-A loads batched, five stale vmcnt(0) waits dropped, attention ticket drawn one unit ahead
# speedup vs baseline: 1.0048x; 1.0014x over previous
.LBB0_276:
	s_and_b64 vcc, exec, s[0:1]
	s_cbranch_vccz .LBB0_265
	v_readlane_b32 s0, v255, 4
	v_mbcnt_lo_u32_b32 v1, -1, 0
	v_mbcnt_hi_u32_b32 v1, -1, v1
	s_nop 1
	v_add_u32_e32 v168, s0, v1
	s_nop 0
	v_cmp_eq_u32_e64 s[0:1], 0, v168
	s_barrier
	s_and_saveexec_b64 s[4:5], s[0:1]
	s_cbranch_execz .LBB0_281
	s_mov_b64 s[8:9], exec
	v_mbcnt_lo_u32_b32 v1, s8, 0
	v_mbcnt_hi_u32_b32 v1, s9, v1
	v_cmp_eq_u32_e32 vcc, 0, v1
	s_and_saveexec_b64 s[6:7], vcc
	s_cbranch_execz .LBB0_280
	s_bcnt1_i32_b64 s8, s[8:9]
	v_mov_b32_e32 v2, s8
	global_atomic_add v2, v0, v2, s[90:91] offset:1280 sc0
	s_waitcnt vmcnt(0)
	v_writelane_b32 v255, 1, 60
	s_mov_b64 s[100:101], exec
	s_mov_b32 exec_lo, 0
	s_mov_b32 exec_hi, 0x10000000
	global_atomic_add v255, v0, v255, s[90:91] offset:1280 sc0
	s_mov_b64 exec, s[100:101]
.LBB0_280:
	s_or_b64 exec, exec, s[6:7]
	s_waitcnt vmcnt(1)
	v_readfirstlane_b32 s6, v2
	v_mov_b32_e32 v2, s96
	s_nop 0
	v_add_u32_e32 v1, s6, v1
	ds_write_b32 v2, v1

.LBB0_283:
	s_or_b64 exec, exec, s[8:9]
	s_waitcnt vmcnt(1)
	v_readfirstlane_b32 s8, v2
	v_mov_b32_e32 v2, s96
	s_nop 0
	v_add_u32_e32 v1, s8, v1
	ds_write_b32 v2, v1

.LBB0_316:
	v_lshl_add_u64 v[2:3], s[56:57], 0, v[110:111]
	s_lshl_b32 s62, s42, 1
	v_lshl_add_u64 v[2:3], v[2:3], 0, s[62:63]
	v_mov_b32_e32 v109, v0
	v_lshl_add_u64 v[6:7], v[2:3], 0, v[108:109]
	v_cvt_pk_bf16_f32 v2, v32, v33
	v_cvt_pk_bf16_f32 v3, v34, v35
	v_cvt_pk_bf16_f32 v4, v36, v37
	v_cvt_pk_bf16_f32 v5, v38, v39
	s_nop 0
	v_permlane32_swap_b32_e32 v2, v4
	v_permlane32_swap_b32_e32 v3, v5
	global_store_dwordx4 v[6:7], v[2:5], off
	s_nop 1
	v_cvt_pk_bf16_f32 v2, v40, v41
	v_cvt_pk_bf16_f32 v3, v42, v43
	v_cvt_pk_bf16_f32 v4, v44, v45
	v_cvt_pk_bf16_f32 v5, v46, v47
	s_nop 0
	v_permlane32_swap_b32_e32 v2, v4
	v_permlane32_swap_b32_e32 v3, v5
	global_store_dwordx4 v[6:7], v[2:5], off offset:32
	s_nop 1
	v_cvt_pk_bf16_f32 v2, v16, v17
	v_cvt_pk_bf16_f32 v3, v18, v19
	v_cvt_pk_bf16_f32 v4, v20, v21
	v_cvt_pk_bf16_f32 v5, v22, v23
	s_nop 0
	v_permlane32_swap_b32_e32 v2, v4
	v_permlane32_swap_b32_e32 v3, v5
	global_store_dwordx4 v[6:7], v[2:5], off offset:64
	s_nop 1
	v_cvt_pk_bf16_f32 v2, v24, v25
	v_cvt_pk_bf16_f32 v3, v26, v27
	v_cvt_pk_bf16_f32 v4, v28, v29
	v_cvt_pk_bf16_f32 v5, v30, v31
	s_nop 0
	v_permlane32_swap_b32_e32 v2, v4
	v_permlane32_swap_b32_e32 v3, v5
	global_store_dwordx4 v[6:7], v[2:5], off offset:96
	s_barrier
	s_and_saveexec_b64 s[6:7], s[0:1]
	s_cbranch_execz .LBB0_284
	s_mov_b64 s[10:11], exec
	v_mbcnt_lo_u32_b32 v1, s10, 0
	v_mbcnt_hi_u32_b32 v1, s11, v1
	v_cmp_eq_u32_e32 vcc, 0, v1
	s_and_saveexec_b64 s[8:9], vcc
	s_cbranch_execz .LBB0_283
	s_bcnt1_i32_b64 s10, s[10:11]
	v_mov_b32_e32 v2, s10
	s_waitcnt vmcnt(0)
	v_readlane_b32 s98, v255, 60
	s_nop 1
	v_mov_b32_e32 v2, s98
	v_writelane_b32 v255, 1, 60
	s_mov_b64 s[100:101], exec
	s_mov_b32 exec_lo, 0
	s_mov_b32 exec_hi, 0x10000000
	global_atomic_add v255, v0, v255, s[90:91] offset:1280 sc0
	s_mov_b64 exec, s[100:101]
	s_branch .LBB0_283

.LBB0_336:
	s_barrier
	s_and_saveexec_b64 s[40:41], s[0:1]
	s_cbranch_execz .LBB0_340
	s_mov_b64 s[68:69], exec
	v_mbcnt_lo_u32_b32 v1, s68, 0
	v_mbcnt_hi_u32_b32 v1, s69, v1
	v_cmp_eq_u32_e32 vcc, 0, v1
	s_and_saveexec_b64 s[66:67], vcc
	s_cbranch_execz .LBB0_339
	s_bcnt1_i32_b64 s33, s[68:69]
	v_mov_b32_e32 v2, s33
	s_waitcnt vmcnt(0)
	v_readlane_b32 s98, v255, 60
	s_nop 1
	v_mov_b32_e32 v2, s98
	v_writelane_b32 v255, 1, 60
	s_mov_b64 s[100:101], exec
	s_mov_b32 exec_lo, 0
	s_mov_b32 exec_hi, 0x10000000
	global_atomic_add v255, v0, v255, s[90:91] offset:1280 sc0
	s_mov_b64 exec, s[100:101]
.LBB0_339:
	s_or_b64 exec, exec, s[66:67]
	s_waitcnt vmcnt(1)
	v_readfirstlane_b32 s33, v2
	v_mov_b32_e32 v2, s96
	s_nop 0
	v_add_u32_e32 v1, s33, v1
	ds_write_b32 v2, v1
